# speedup vs baseline: 1.0828x; 1.0295x over previous
.Lp_w1t:
	s_load_dwordx2 s[16:17], s[0:1], 0x38
	s_load_dwordx2 s[18:19], s[0:1], 0x40
	s_load_dwordx4 s[20:23], s[0:1], 0x48
	v_lshl_or_b32 v2, s2, 8, v0
	v_add_u32_e32 v2, 0xfffec000, v2
	v_mov_b32_e32 v3, 0
	v_mov_b32_e32 v26, v0
	v_lshrrev_b32_e32 v4, 3, v2
	v_lshrrev_b32_e32 v5, 3, v0
	v_lshlrev_b32_e32 v0, 1, v0
	v_and_b32_e32 v4, 0x1fffffe0, v4
	v_and_b32_e32 v6, 0x80, v0
	v_mov_b32_e32 v7, 0
	v_and_or_b32 v4, v5, 20, v4
	s_waitcnt lgkmcnt(0)
	v_lshl_add_u64 v[8:9], s[8:9], 0, v[6:7]
	v_lshlrev_b32_e32 v6, 2, v1
	v_lshl_add_u64 v[0:1], v[8:9], 0, v[6:7]
	v_or_b32_e32 v6, 1, v4
	v_lshlrev_b64 v[10:11], 8, v[6:7]
	v_or_b32_e32 v6, 2, v4
	v_lshlrev_b64 v[12:13], 8, v[6:7]
	v_or_b32_e32 v6, 3, v4
	v_lshlrev_b64 v[14:15], 8, v[6:7]
	v_or_b32_e32 v6, 8, v4
	v_lshlrev_b64 v[16:17], 8, v[6:7]
	v_or_b32_e32 v6, 9, v4
	v_mov_b32_e32 v5, v7
	v_lshlrev_b64 v[18:19], 8, v[6:7]
	v_or_b32_e32 v6, 10, v4
	v_lshlrev_b64 v[8:9], 8, v[4:5]
	v_lshlrev_b64 v[20:21], 8, v[6:7]
	v_or_b32_e32 v6, 11, v4
	v_lshl_add_u64 v[8:9], v[0:1], 0, v[8:9]
	v_lshlrev_b64 v[4:5], 8, v[6:7]
	v_lshl_add_u64 v[10:11], v[0:1], 0, v[10:11]
	v_lshl_add_u64 v[12:13], v[0:1], 0, v[12:13]
	v_lshl_add_u64 v[14:15], v[0:1], 0, v[14:15]
	v_lshl_add_u64 v[16:17], v[0:1], 0, v[16:17]
	v_lshl_add_u64 v[18:19], v[0:1], 0, v[18:19]
	v_lshl_add_u64 v[20:21], v[0:1], 0, v[20:21]
	v_lshl_add_u64 v[0:1], v[0:1], 0, v[4:5]
	global_load_dword v4, v[8:9], off
	global_load_dword v5, v[10:11], off
	global_load_dword v6, v[12:13], off
	global_load_dword v7, v[14:15], off
	global_load_dword v22, v[16:17], off
	global_load_dword v23, v[18:19], off
	global_load_dword v24, v[20:21], off
	global_load_dword v25, v[0:1], off
	v_lshl_add_u64 v[0:1], v[2:3], 4, s[16:17]
	s_getpc_b64 s[24:25]
	s_and_b32 s24, s24, 0xfffff000
	v_lshlrev_b32_e32 v32, 7, v26
	v_mov_b32_e32 v33, 0
	v_lshl_add_u64 v[34:35], s[24:25], 0, v[32:33]
	global_load_dword v31, v[34:35], off sc0 sc1
	s_waitcnt vmcnt(1)
	v_cvt_pk_f16_f32 v4, v4, v5
	v_cvt_pk_f16_f32 v5, v6, v7
	v_cvt_pk_f16_f32 v6, v22, v23
	v_cvt_pk_f16_f32 v7, v24, v25
	global_store_dwordx4 v[0:1], v[4:7], off sc1
	s_movk_i32 s4, 0x70
	v_cmp_gt_u32_e32 vcc, s4, v26
	s_and_saveexec_b64 s[4:5], vcc
	s_cbranch_execz .Lp_t1
	v_add_co_u32_e32 v34, vcc, 0x8000, v34
	s_nop 1
	v_addc_co_u32_e32 v35, vcc, 0, v35, vcc
	global_load_dword v8, v[34:35], off sc0 sc1

amdhsa.kernels:
  - .agpr_count:     16
    .args:
      - .actual_access:  read_only
        .address_space:  global
        .offset:         0
        .size:           8
        .value_kind:     global_buffer
      - .actual_access:  read_only
        .address_space:  global
        .offset:         8
        .size:           8
        .value_kind:     global_buffer
      - .actual_access:  read_only
        .address_space:  global
        .offset:         16
        .size:           8
        .value_kind:     global_buffer
      - .actual_access:  read_only
        .address_space:  global
        .offset:         24
        .size:           8
        .value_kind:     global_buffer
      - .actual_access:  write_only
        .address_space:  global
        .offset:         32
        .size:           8
        .value_kind:     global_buffer
      - .actual_access:  write_only
        .address_space:  global
        .offset:         40
        .size:           8
        .value_kind:     global_buffer
      - .actual_access:  write_only
        .address_space:  global
        .offset:         48
        .size:           8
        .value_kind:     global_buffer
      - .actual_access:  write_only
        .address_space:  global
        .offset:         56
        .size:           8
        .value_kind:     global_buffer
      - .actual_access:  read_only
        .address_space:  global
        .offset:         64
        .size:           8
        .value_kind:     global_buffer
      - .actual_access:  read_only
        .address_space:  global
        .offset:         72
        .size:           8
        .value_kind:     global_buffer
      - .actual_access:  read_only
        .address_space:  global
        .offset:         80
        .size:           8
        .value_kind:     global_buffer
    .group_segment_fixed_size: 33792
    .kernarg_segment_align: 8
    .kernarg_segment_size: 88
    .language:       OpenCL C
    .language_version:
      - 2
      - 0
    .max_flat_workgroup_size: 256
    .name:           _Z6k_prepPKfS0_S0_S0_PDF16_S1_S1_S1_S0_S0_S0_
    .private_segment_fixed_size: 0
    .sgpr_count:     22
    .sgpr_spill_count: 0
    .symbol:         _Z6k_prepPKfS0_S0_S0_PDF16_S1_S1_S1_S0_S0_S0_.kd
    .uniform_work_group_size: 1
    .uses_dynamic_stack: false
    .vgpr_count:     200
    .vgpr_spill_count: 0
    .wavefront_size: 64
  - .agpr_count:     0
    .args:
      - .actual_access:  read_only
        .address_space:  global
        .offset:         0
        .size:           8
        .value_kind:     global_buffer
      - .actual_access:  read_only
        .address_space:  global
        .offset:         8
        .size:           8
        .value_kind:     global_buffer
      - .actual_access:  read_only
        .address_space:  global
        .offset:         16
        .size:           8
        .value_kind:     global_buffer
      - .actual_access:  write_only
        .address_space:  global
        .offset:         24
        .size:           8
        .value_kind:     global_buffer
    .group_segment_fixed_size: 0
    .kernarg_segment_align: 8
    .kernarg_segment_size: 32
    .language:       OpenCL C
    .language_version:
      - 2
      - 0
    .max_flat_workgroup_size: 128
    .name:           _Z7k_finalPKfS0_S0_Pf
    .private_segment_fixed_size: 0
    .sgpr_count:     18
    .sgpr_spill_count: 0
    .symbol:         _Z7k_finalPKfS0_S0_Pf.kd
    .uniform_work_group_size: 1
    .uses_dynamic_stack: false
    .vgpr_count:     78
    .vgpr_spill_count: 0
    .wavefront_size: 64
  - .agpr_count:     0
    .args:
      - .actual_access:  read_only
        .address_space:  global
        .offset:         0
        .size:           8
        .value_kind:     global_buffer
      - .actual_access:  read_only
        .address_space:  global
        .offset:         8
        .size:           8
        .value_kind:     global_buffer
      - .actual_access:  read_only
        .address_space:  global
        .offset:         16
        .size:           8
        .value_kind:     global_buffer
      - .actual_access:  read_only
        .address_space:  global
        .offset:         24
        .size:           8
        .value_kind:     global_buffer
      - .actual_access:  read_only
        .address_space:  global
        .offset:         32
        .size:           8
        .value_kind:     global_buffer
      - .actual_access:  write_only
        .address_space:  global
        .offset:         40
        .size:           8
        .value_kind:     global_buffer
      - .actual_access:  write_only
        .address_space:  global
        .offset:         48
        .size:           8
        .value_kind:     global_buffer
      - .actual_access:  read_only
        .address_space:  global
        .offset:         56
        .size:           8
        .value_kind:     global_buffer
      - .actual_access:  read_only
        .address_space:  global
        .offset:         64
        .size:           8
        .value_kind:     global_buffer
    .group_segment_fixed_size: 33808
    .kernarg_segment_align: 8
    .kernarg_segment_size: 72
    .language:       OpenCL C
    .language_version:
      - 2
      - 0
    .max_flat_workgroup_size: 384
    .name:           _Z6k_gemmILi0EEvPKDF16_S1_PKfS3_S1_PDF16_PfS1_S5_
    .private_segment_fixed_size: 0
    .sgpr_count:     20
    .sgpr_spill_count: 0
    .symbol:         _Z6k_gemmILi0EEvPKDF16_S1_PKfS3_S1_PDF16_PfS1_S5_.kd
    .uniform_work_group_size: 1
    .uses_dynamic_stack: false
    .vgpr_count:     150
    .vgpr_spill_count: 0
    .wavefront_size: 64
  - .agpr_count:     0
    .args:
      - .actual_access:  read_only
        .address_space:  global
        .offset:         0
        .size:           8
        .value_kind:     global_buffer
      - .actual_access:  read_only
        .address_space:  global
        .offset:         8
        .size:           8
        .value_kind:     global_buffer
      - .actual_access:  read_only
        .address_space:  global
        .offset:         16
        .size:           8
        .value_kind:     global_buffer
      - .actual_access:  read_only
        .address_space:  global
        .offset:         24
        .size:           8
        .value_kind:     global_buffer
      - .actual_access:  read_only
        .address_space:  global
        .offset:         32
        .size:           8
        .value_kind:     global_buffer
      - .actual_access:  read_only
        .address_space:  global
        .offset:         40
        .size:           8
        .value_kind:     global_buffer
      - .actual_access:  read_only
        .address_space:  global
        .offset:         48
        .size:           8
        .value_kind:     global_buffer
      - .actual_access:  read_only
        .address_space:  global
        .offset:         56
        .size:           8
        .value_kind:     global_buffer
      - .actual_access:  write_only
        .address_space:  global
        .offset:         64
        .size:           8
        .value_kind:     global_buffer
    .group_segment_fixed_size: 50176
    .kernarg_segment_align: 8
    .kernarg_segment_size: 72
    .language:       OpenCL C
    .language_version:
      - 2
      - 0
    .max_flat_workgroup_size: 384
    .name:           _Z6k_gemmILi1EEvPKDF16_S1_PKfS3_S1_PDF16_PfS1_S5_
    .private_segment_fixed_size: 0
    .sgpr_count:     20
    .sgpr_spill_count: 0
    .symbol:         _Z6k_gemmILi1EEvPKDF16_S1_PKfS3_S1_PDF16_PfS1_S5_.kd
    .uniform_work_group_size: 1
    .uses_dynamic_stack: false
    .vgpr_count:     182
    .vgpr_spill_count: 0
    .wavefront_size: 64
